# v70 + counted vmcnt(15..0) waits in the SGU input unpack (16 row loads consumed in issue order) instead of one vmcnt(0)
# baseline (speedup 1.0000x reference)
.LBB0_456:
	s_mov_b64 s[16:17], s[0:1]
	s_load_dwordx2 s[10:11], s[16:17], 0xd0
	v_mbcnt_lo_u32_b32 v0, -1, 0
	v_mbcnt_hi_u32_b32 v0, -1, v0
	v_mov_b32_e32 v5, v1
	v_add_u32_e32 v87, s67, v0
	s_waitcnt lgkmcnt(0)
	s_add_u32 s14, s10, 0xbc00000
	v_bfe_u32 v0, v87, 3, 3
	v_readfirstlane_b32 s4, v87
	v_lshl_add_u64 v[2:3], s[8:9], 0, v[0:1]
	s_addc_u32 s15, s11, 0
	s_and_b32 s6, s4, 0xffffffc0
	v_lshlrev_b64 v[2:3], 11, v[2:3]
	v_and_b32_e32 v144, 7, v87
	s_ashr_i32 s7, s6, 31
	v_lshl_add_u64 v[2:3], s[14:15], 0, v[2:3]
	v_lshlrev_b32_e32 v4, 4, v144
	v_lshl_add_u64 v[2:3], s[6:7], 1, v[2:3]
	v_lshl_add_u64 v[2:3], v[2:3], 0, v[4:5]
	s_mov_b32 s5, 0xfffc5000
	v_add_co_u32_e32 v4, vcc, s5, v2
	s_mov_b32 s5, 0xfffc9000
	s_nop 0
	v_addc_co_u32_e32 v5, vcc, -1, v3, vcc
	global_load_dwordx4 v[62:65], v[4:5], off offset:-3072
	v_add_co_u32_e32 v4, vcc, s5, v2
	s_mov_b32 s5, 0xfffcd000
	s_nop 0
	v_addc_co_u32_e32 v5, vcc, -1, v3, vcc
	v_add_co_u32_e32 v6, vcc, s5, v2
	s_mov_b32 s5, 0xfffd1000
	s_nop 0
	v_addc_co_u32_e32 v7, vcc, -1, v3, vcc
	global_load_dwordx4 v[58:61], v[4:5], off offset:-3072
	global_load_dwordx4 v[54:57], v[6:7], off offset:-3072
	v_add_co_u32_e32 v4, vcc, s5, v2
	s_mov_b32 s5, 0xfffd5000
	s_nop 0
	v_addc_co_u32_e32 v5, vcc, -1, v3, vcc
	v_add_co_u32_e32 v6, vcc, s5, v2
	s_mov_b32 s5, 0xfffd9000
	s_nop 0
	v_addc_co_u32_e32 v7, vcc, -1, v3, vcc
	global_load_dwordx4 v[50:53], v[4:5], off offset:-3072
	global_load_dwordx4 v[46:49], v[6:7], off offset:-3072
	v_add_co_u32_e32 v4, vcc, s5, v2
	s_mov_b32 s5, 0xfffdd000
	s_nop 0
	v_addc_co_u32_e32 v5, vcc, -1, v3, vcc
	v_add_co_u32_e32 v6, vcc, s5, v2
	s_mov_b32 s5, 0xfffe1000
	s_nop 0
	v_addc_co_u32_e32 v7, vcc, -1, v3, vcc
	global_load_dwordx4 v[42:45], v[4:5], off offset:-3072
	global_load_dwordx4 v[38:41], v[6:7], off offset:-3072
	v_add_co_u32_e32 v4, vcc, s5, v2
	s_mov_b32 s5, 0xfffe5000
	s_nop 0
	v_addc_co_u32_e32 v5, vcc, -1, v3, vcc
	v_add_co_u32_e32 v6, vcc, s5, v2
	s_mov_b32 s5, 0xfffe9000
	s_nop 0
	v_addc_co_u32_e32 v7, vcc, -1, v3, vcc
	global_load_dwordx4 v[34:37], v[4:5], off offset:-3072
	global_load_dwordx4 v[30:33], v[6:7], off offset:-3072
	v_add_co_u32_e32 v4, vcc, s5, v2
	s_mov_b32 s5, 0xfffed000
	s_nop 0
	v_addc_co_u32_e32 v5, vcc, -1, v3, vcc
	v_add_co_u32_e32 v6, vcc, s5, v2
	s_mov_b32 s5, 0xffff1000
	s_nop 0
	v_addc_co_u32_e32 v7, vcc, -1, v3, vcc
	global_load_dwordx4 v[26:29], v[4:5], off offset:-3072
	global_load_dwordx4 v[22:25], v[6:7], off offset:-3072
	v_add_co_u32_e32 v4, vcc, s5, v2
	s_mov_b32 s5, 0xffff5000
	s_nop 0
	v_addc_co_u32_e32 v5, vcc, -1, v3, vcc
	v_add_co_u32_e32 v6, vcc, s5, v2
	s_movk_i32 s5, 0x9000
	s_nop 0
	v_addc_co_u32_e32 v7, vcc, -1, v3, vcc
	global_load_dwordx4 v[18:21], v[4:5], off offset:-3072
	global_load_dwordx4 v[14:17], v[6:7], off offset:-3072
	v_add_co_u32_e32 v4, vcc, s5, v2
	s_movk_i32 s5, 0xd000
	s_nop 0
	v_addc_co_u32_e32 v5, vcc, -1, v3, vcc
	v_add_co_u32_e32 v6, vcc, s5, v2
	v_and_b32_e32 v67, 64, v234
	s_nop 0
	v_addc_co_u32_e32 v7, vcc, -1, v3, vcc
	global_load_dwordx4 v[10:13], v[4:5], off offset:-3072
	s_nop 0
	global_load_dwordx4 v[6:9], v[6:7], off offset:-3072
	s_nop 0
	global_load_dwordx4 v[2:5], v[2:3], off offset:1024
	v_xor_b32_e32 v66, 1, v234
	v_add_u32_e32 v104, 64, v67
	s_waitcnt vmcnt(15)
	v_and_b32_e32 v151, 0xffff0000, v62
	v_and_b32_e32 v153, 0xffff0000, v63
	v_lshlrev_b32_e32 v152, 16, v62
	v_mul_f32_e32 v62, v151, v151
	v_lshlrev_b32_e32 v154, 16, v63
	v_mul_f32_e32 v63, v153, v153
	v_fmac_f32_e32 v62, v152, v152
	v_fmac_f32_e32 v63, v154, v154
	v_and_b32_e32 v155, 0xffff0000, v64
	v_add_f32_e32 v62, v62, v63
	v_lshlrev_b32_e32 v156, 16, v64
	v_mul_f32_e32 v63, v155, v155
	v_fmac_f32_e32 v63, v156, v156
	v_and_b32_e32 v157, 0xffff0000, v65
	v_cmp_lt_i32_e32 vcc, v66, v104
	v_add_f32_e32 v62, v63, v62
	v_lshlrev_b32_e32 v158, 16, v65
	v_mul_f32_e32 v63, v157, v157
	v_cndmask_b32_e32 v66, v234, v66, vcc
	v_fmac_f32_e32 v63, v158, v158
	v_lshlrev_b32_e32 v102, 2, v66
	v_add_f32_e32 v62, v63, v62
	s_nop 1
	v_add_f32_dpp v62, v62, v62 quad_perm:[1,0,3,2] row_mask:0xf bank_mask:0xf
	s_nop 1
	v_add_f32_dpp v62, v62, v62 quad_perm:[2,3,0,1] row_mask:0xf bank_mask:0xf
	s_nop 1
	v_mov_b32_e32 v63, v62
	s_nop 1
	v_add_f32_dpp v62, v63, v62 row_shl:4 row_mask:0xf bank_mask:0x5
	s_nop 1
	v_add_f32_dpp v62, v63, v62 row_shr:4 row_mask:0xf bank_mask:0xa
	s_nop 1
	v_mov_b32_e32 v63, 0
	v_xor_b32_e32 v66, 2, v234
	v_cmp_lt_i32_e32 vcc, v66, v104
	s_ashr_i32 s12, s4, 6
	s_lshl_b32 s4, s12, 2
	v_cndmask_b32_e32 v64, v234, v66, vcc
	v_lshlrev_b32_e32 v101, 2, v64
	s_waitcnt lgkmcnt(0)
	v_add_f32_e32 v62, v62, v63
	v_mov_b32_e32 v63, 0
	v_xor_b32_e32 v64, 4, v234
	v_cmp_lt_i32_e32 vcc, v64, v104
	s_add_i32 s4, s4, 0
	s_add_i32 s4, s4, 0x22000
	v_cndmask_b32_e32 v64, v234, v64, vcc
	v_lshlrev_b32_e32 v100, 2, v64
	s_waitcnt lgkmcnt(0)
	v_add_f32_e32 v62, v62, v63
	v_mov_b32_e32 v63, 0
	v_and_b32_e32 v64, 56, v87
	v_cmp_eq_u32_e32 vcc, 0, v144
	v_lshl_add_u32 v103, v64, 2, s4
	s_and_saveexec_b64 s[18:19], vcc
	s_cbranch_execz .LBB0_458
	s_waitcnt lgkmcnt(0)
	v_add_f32_e32 v62, v62, v63
	ds_write_b32 v103, v62
.LBB0_458:
	s_or_b64 exec, exec, s[18:19]
	s_waitcnt vmcnt(14)
	v_and_b32_e32 v135, 0xffff0000, v58
	v_and_b32_e32 v137, 0xffff0000, v59
	v_lshlrev_b32_e32 v136, 16, v58
	v_mul_f32_e32 v58, v135, v135
	v_lshlrev_b32_e32 v138, 16, v59
	v_mul_f32_e32 v59, v137, v137
	v_fmac_f32_e32 v58, v136, v136
	v_fmac_f32_e32 v59, v138, v138
	v_and_b32_e32 v139, 0xffff0000, v60
	v_add_f32_e32 v58, v58, v59
	v_lshlrev_b32_e32 v140, 16, v60
	v_mul_f32_e32 v59, v139, v139
	v_fmac_f32_e32 v59, v140, v140
	v_and_b32_e32 v141, 0xffff0000, v61
	v_add_f32_e32 v58, v59, v58
	v_lshlrev_b32_e32 v142, 16, v61
	v_mul_f32_e32 v59, v141, v141
	v_fmac_f32_e32 v59, v142, v142
	v_add_f32_e32 v58, v59, v58
	s_nop 1
	v_add_f32_dpp v58, v58, v58 quad_perm:[1,0,3,2] row_mask:0xf bank_mask:0xf
	s_nop 1
	v_add_f32_dpp v58, v58, v58 quad_perm:[2,3,0,1] row_mask:0xf bank_mask:0xf
	s_nop 1
	v_mov_b32_e32 v59, v58
	s_nop 1
	v_add_f32_dpp v58, v59, v58 row_shl:4 row_mask:0xf bank_mask:0x5
	s_nop 1
	v_add_f32_dpp v58, v59, v58 row_shr:4 row_mask:0xf bank_mask:0xa
	s_nop 1
	v_mov_b32_e32 v59, 0
	s_load_dwordx2 s[18:19], s[16:17], 0x30
	s_nop 0
	s_load_dwordx2 s[16:17], s[16:17], 0x40
	s_waitcnt lgkmcnt(0)
	v_add_f32_e32 v58, v58, v59
	v_mov_b32_e32 v59, 0
	s_waitcnt lgkmcnt(0)
	v_add_f32_e32 v58, v58, v59
	v_mov_b32_e32 v59, 0
	s_and_saveexec_b64 s[20:21], vcc
	s_cbranch_execz .LBB0_460
	s_waitcnt lgkmcnt(0)
	v_add_f32_e32 v58, v58, v59
	ds_write_b32 v103, v58 offset:256
.LBB0_460:
	s_or_b64 exec, exec, s[20:21]
	s_waitcnt vmcnt(13)
	v_and_b32_e32 v123, 0xffff0000, v54
	v_and_b32_e32 v125, 0xffff0000, v55
	v_lshlrev_b32_e32 v124, 16, v54
	v_mul_f32_e32 v54, v123, v123
	v_lshlrev_b32_e32 v126, 16, v55
	v_mul_f32_e32 v55, v125, v125
	v_fmac_f32_e32 v54, v124, v124
	v_fmac_f32_e32 v55, v126, v126
	v_and_b32_e32 v127, 0xffff0000, v56
	v_add_f32_e32 v54, v54, v55
	v_lshlrev_b32_e32 v129, 16, v56
	v_mul_f32_e32 v55, v127, v127
	v_fmac_f32_e32 v55, v129, v129
	v_and_b32_e32 v130, 0xffff0000, v57
	v_add_f32_e32 v54, v55, v54
	v_lshlrev_b32_e32 v131, 16, v57
	v_mul_f32_e32 v55, v130, v130
	v_fmac_f32_e32 v55, v131, v131
	v_add_f32_e32 v54, v55, v54
	s_nop 1
	v_add_f32_dpp v54, v54, v54 quad_perm:[1,0,3,2] row_mask:0xf bank_mask:0xf
	s_nop 1
	v_add_f32_dpp v54, v54, v54 quad_perm:[2,3,0,1] row_mask:0xf bank_mask:0xf
	s_nop 1
	v_mov_b32_e32 v55, v54
	s_nop 1
	v_add_f32_dpp v54, v55, v54 row_shl:4 row_mask:0xf bank_mask:0x5
	s_nop 1
	v_add_f32_dpp v54, v55, v54 row_shr:4 row_mask:0xf bank_mask:0xa
	s_nop 1
	v_mov_b32_e32 v55, 0
	s_waitcnt lgkmcnt(0)
	v_add_f32_e32 v54, v54, v55
	v_mov_b32_e32 v55, 0
	s_waitcnt lgkmcnt(0)
	v_add_f32_e32 v54, v54, v55
	v_mov_b32_e32 v55, 0
	s_and_saveexec_b64 s[20:21], vcc
	s_cbranch_execz .LBB0_462
	s_waitcnt lgkmcnt(0)
	v_add_f32_e32 v54, v54, v55
	ds_write_b32 v103, v54 offset:512
.LBB0_462:
	s_or_b64 exec, exec, s[20:21]
	s_waitcnt vmcnt(12)
	v_and_b32_e32 v115, 0xffff0000, v50
	v_and_b32_e32 v117, 0xffff0000, v51
	v_lshlrev_b32_e32 v116, 16, v50
	v_mul_f32_e32 v50, v115, v115
	v_lshlrev_b32_e32 v118, 16, v51
	v_mul_f32_e32 v51, v117, v117
	v_fmac_f32_e32 v50, v116, v116
	v_fmac_f32_e32 v51, v118, v118
	v_and_b32_e32 v119, 0xffff0000, v52
	v_add_f32_e32 v50, v50, v51
	v_lshlrev_b32_e32 v120, 16, v52
	v_mul_f32_e32 v51, v119, v119
	v_fmac_f32_e32 v51, v120, v120
	v_and_b32_e32 v121, 0xffff0000, v53
	v_add_f32_e32 v50, v51, v50
	v_lshlrev_b32_e32 v122, 16, v53
	v_mul_f32_e32 v51, v121, v121
	v_fmac_f32_e32 v51, v122, v122
	v_add_f32_e32 v50, v51, v50
	s_nop 1
	v_add_f32_dpp v50, v50, v50 quad_perm:[1,0,3,2] row_mask:0xf bank_mask:0xf
	s_nop 1
	v_add_f32_dpp v50, v50, v50 quad_perm:[2,3,0,1] row_mask:0xf bank_mask:0xf
	s_nop 1
	v_mov_b32_e32 v51, v50
	s_nop 1
	v_add_f32_dpp v50, v51, v50 row_shl:4 row_mask:0xf bank_mask:0x5
	s_nop 1
	v_add_f32_dpp v50, v51, v50 row_shr:4 row_mask:0xf bank_mask:0xa
	s_nop 1
	v_mov_b32_e32 v51, 0
	s_waitcnt lgkmcnt(0)
	v_add_f32_e32 v50, v50, v51
	v_mov_b32_e32 v51, 0
	s_waitcnt lgkmcnt(0)
	v_add_f32_e32 v50, v50, v51
	v_mov_b32_e32 v51, 0
	s_and_saveexec_b64 s[20:21], vcc
	s_cbranch_execz .LBB0_464
	s_waitcnt lgkmcnt(0)
	v_add_f32_e32 v50, v50, v51
	ds_write_b32 v103, v50 offset:768
.LBB0_464:
	s_or_b64 exec, exec, s[20:21]
	s_waitcnt vmcnt(11)
	v_and_b32_e32 v107, 0xffff0000, v46
	v_and_b32_e32 v109, 0xffff0000, v47
	v_lshlrev_b32_e32 v108, 16, v46
	v_mul_f32_e32 v46, v107, v107
	v_lshlrev_b32_e32 v110, 16, v47
	v_mul_f32_e32 v47, v109, v109
	v_fmac_f32_e32 v46, v108, v108
	v_fmac_f32_e32 v47, v110, v110
	v_and_b32_e32 v111, 0xffff0000, v48
	v_add_f32_e32 v46, v46, v47
	v_lshlrev_b32_e32 v112, 16, v48
	v_mul_f32_e32 v47, v111, v111
	v_fmac_f32_e32 v47, v112, v112
	v_and_b32_e32 v113, 0xffff0000, v49
	v_add_f32_e32 v46, v47, v46
	v_lshlrev_b32_e32 v114, 16, v49
	v_mul_f32_e32 v47, v113, v113
	v_fmac_f32_e32 v47, v114, v114
	v_add_f32_e32 v46, v47, v46
	s_nop 1
	v_add_f32_dpp v46, v46, v46 quad_perm:[1,0,3,2] row_mask:0xf bank_mask:0xf
	s_nop 1
	v_add_f32_dpp v46, v46, v46 quad_perm:[2,3,0,1] row_mask:0xf bank_mask:0xf
	s_nop 1
	v_mov_b32_e32 v47, v46
	s_nop 1
	v_add_f32_dpp v46, v47, v46 row_shl:4 row_mask:0xf bank_mask:0x5
	s_nop 1
	v_add_f32_dpp v46, v47, v46 row_shr:4 row_mask:0xf bank_mask:0xa
	s_nop 1
	v_mov_b32_e32 v47, 0
	s_waitcnt lgkmcnt(0)
	v_add_f32_e32 v46, v46, v47
	v_mov_b32_e32 v47, 0
	s_waitcnt lgkmcnt(0)
	v_add_f32_e32 v46, v46, v47
	v_mov_b32_e32 v47, 0
	s_and_saveexec_b64 s[20:21], vcc
	s_cbranch_execz .LBB0_466
	s_waitcnt lgkmcnt(0)
	v_add_f32_e32 v46, v46, v47
	ds_write_b32 v103, v46 offset:1024
.LBB0_466:
	s_or_b64 exec, exec, s[20:21]
	s_waitcnt vmcnt(10)
	v_and_b32_e32 v92, 0xffff0000, v42
	v_and_b32_e32 v94, 0xffff0000, v43
	v_lshlrev_b32_e32 v93, 16, v42
	v_mul_f32_e32 v42, v92, v92
	v_lshlrev_b32_e32 v95, 16, v43
	v_mul_f32_e32 v43, v94, v94
	v_fmac_f32_e32 v42, v93, v93
	v_fmac_f32_e32 v43, v95, v95
	v_and_b32_e32 v96, 0xffff0000, v44
	v_add_f32_e32 v42, v42, v43
	v_lshlrev_b32_e32 v97, 16, v44
	v_mul_f32_e32 v43, v96, v96
	v_fmac_f32_e32 v43, v97, v97
	v_and_b32_e32 v98, 0xffff0000, v45
	v_add_f32_e32 v42, v43, v42
	v_lshlrev_b32_e32 v99, 16, v45
	v_mul_f32_e32 v43, v98, v98
	v_fmac_f32_e32 v43, v99, v99
	v_add_f32_e32 v42, v43, v42
	s_nop 1
	v_add_f32_dpp v42, v42, v42 quad_perm:[1,0,3,2] row_mask:0xf bank_mask:0xf
	s_nop 1
	v_add_f32_dpp v42, v42, v42 quad_perm:[2,3,0,1] row_mask:0xf bank_mask:0xf
	s_nop 1
	v_mov_b32_e32 v43, v42
	s_nop 1
	v_add_f32_dpp v42, v43, v42 row_shl:4 row_mask:0xf bank_mask:0x5
	s_nop 1
	v_add_f32_dpp v42, v43, v42 row_shr:4 row_mask:0xf bank_mask:0xa
	s_nop 1
	v_mov_b32_e32 v43, 0
	s_waitcnt lgkmcnt(0)
	v_add_f32_e32 v42, v42, v43
	v_mov_b32_e32 v43, 0
	s_waitcnt lgkmcnt(0)
	v_add_f32_e32 v42, v42, v43
	v_mov_b32_e32 v43, 0
	s_and_saveexec_b64 s[20:21], vcc
	s_cbranch_execz .LBB0_468
	s_waitcnt lgkmcnt(0)
	v_add_f32_e32 v42, v42, v43
	ds_write_b32 v103, v42 offset:1280
.LBB0_468:
	s_or_b64 exec, exec, s[20:21]
	s_waitcnt vmcnt(9)
	v_and_b32_e32 v83, 0xffff0000, v38
	v_and_b32_e32 v85, 0xffff0000, v39
	v_lshlrev_b32_e32 v84, 16, v38
	v_mul_f32_e32 v38, v83, v83
	v_lshlrev_b32_e32 v86, 16, v39
	v_mul_f32_e32 v39, v85, v85
	v_fmac_f32_e32 v38, v84, v84
	v_fmac_f32_e32 v39, v86, v86
	v_and_b32_e32 v88, 0xffff0000, v40
	v_add_f32_e32 v38, v38, v39
	v_lshlrev_b32_e32 v89, 16, v40
	v_mul_f32_e32 v39, v88, v88
	v_fmac_f32_e32 v39, v89, v89
	v_and_b32_e32 v90, 0xffff0000, v41
	v_add_f32_e32 v38, v39, v38
	v_lshlrev_b32_e32 v91, 16, v41
	v_mul_f32_e32 v39, v90, v90
	v_fmac_f32_e32 v39, v91, v91
	v_add_f32_e32 v38, v39, v38
	s_nop 1
	v_add_f32_dpp v38, v38, v38 quad_perm:[1,0,3,2] row_mask:0xf bank_mask:0xf
	s_nop 1
	v_add_f32_dpp v38, v38, v38 quad_perm:[2,3,0,1] row_mask:0xf bank_mask:0xf
	s_nop 1
	v_mov_b32_e32 v39, v38
	s_nop 1
	v_add_f32_dpp v38, v39, v38 row_shl:4 row_mask:0xf bank_mask:0x5
	s_nop 1
	v_add_f32_dpp v38, v39, v38 row_shr:4 row_mask:0xf bank_mask:0xa
	s_nop 1
	v_mov_b32_e32 v39, 0
	s_waitcnt lgkmcnt(0)
	v_add_f32_e32 v38, v38, v39
	v_mov_b32_e32 v39, 0
	s_waitcnt lgkmcnt(0)
	v_add_f32_e32 v38, v38, v39
	v_mov_b32_e32 v39, 0
	s_and_saveexec_b64 s[20:21], vcc
	s_cbranch_execz .LBB0_470
	s_waitcnt lgkmcnt(0)
	v_add_f32_e32 v38, v38, v39
	ds_write_b32 v103, v38 offset:1536
.LBB0_470:
	s_or_b64 exec, exec, s[20:21]
	s_waitcnt vmcnt(8)
	v_and_b32_e32 v75, 0xffff0000, v34
	v_and_b32_e32 v77, 0xffff0000, v35
	v_lshlrev_b32_e32 v76, 16, v34
	v_mul_f32_e32 v34, v75, v75
	v_lshlrev_b32_e32 v78, 16, v35
	v_mul_f32_e32 v35, v77, v77
	v_fmac_f32_e32 v34, v76, v76
	v_fmac_f32_e32 v35, v78, v78
	v_and_b32_e32 v79, 0xffff0000, v36
	v_add_f32_e32 v34, v34, v35
	v_lshlrev_b32_e32 v80, 16, v36
	v_mul_f32_e32 v35, v79, v79
	v_fmac_f32_e32 v35, v80, v80
	v_and_b32_e32 v81, 0xffff0000, v37
	v_add_f32_e32 v34, v35, v34
	v_lshlrev_b32_e32 v82, 16, v37
	v_mul_f32_e32 v35, v81, v81
	v_fmac_f32_e32 v35, v82, v82
	v_add_f32_e32 v34, v35, v34
	s_nop 1
	v_add_f32_dpp v34, v34, v34 quad_perm:[1,0,3,2] row_mask:0xf bank_mask:0xf
	s_nop 1
	v_add_f32_dpp v34, v34, v34 quad_perm:[2,3,0,1] row_mask:0xf bank_mask:0xf
	s_nop 1
	v_mov_b32_e32 v35, v34
	s_nop 1
	v_add_f32_dpp v34, v35, v34 row_shl:4 row_mask:0xf bank_mask:0x5
	s_nop 1
	v_add_f32_dpp v34, v35, v34 row_shr:4 row_mask:0xf bank_mask:0xa
	s_nop 1
	v_mov_b32_e32 v35, 0
	s_waitcnt lgkmcnt(0)
	v_add_f32_e32 v34, v34, v35
	v_mov_b32_e32 v35, 0
	s_waitcnt lgkmcnt(0)
	v_add_f32_e32 v34, v34, v35
	v_mov_b32_e32 v35, 0
	s_and_saveexec_b64 s[20:21], vcc
	s_cbranch_execz .LBB0_472
	s_waitcnt lgkmcnt(0)
	v_add_f32_e32 v34, v34, v35
	ds_write_b32 v103, v34 offset:1792
.LBB0_472:
	s_or_b64 exec, exec, s[20:21]
	s_waitcnt vmcnt(7)
	v_and_b32_e32 v67, 0xffff0000, v30
	v_and_b32_e32 v69, 0xffff0000, v31
	v_lshlrev_b32_e32 v68, 16, v30
	v_mul_f32_e32 v30, v67, v67
	v_lshlrev_b32_e32 v70, 16, v31
	v_mul_f32_e32 v31, v69, v69
	v_fmac_f32_e32 v30, v68, v68
	v_fmac_f32_e32 v31, v70, v70
	v_and_b32_e32 v71, 0xffff0000, v32
	v_add_f32_e32 v30, v30, v31
	v_lshlrev_b32_e32 v72, 16, v32
	v_mul_f32_e32 v31, v71, v71
	v_fmac_f32_e32 v31, v72, v72
	v_and_b32_e32 v73, 0xffff0000, v33
	v_add_f32_e32 v30, v31, v30
	v_lshlrev_b32_e32 v74, 16, v33
	v_mul_f32_e32 v31, v73, v73
	v_fmac_f32_e32 v31, v74, v74
	v_add_f32_e32 v30, v31, v30
	s_nop 1
	v_add_f32_dpp v30, v30, v30 quad_perm:[1,0,3,2] row_mask:0xf bank_mask:0xf
	s_nop 1
	v_add_f32_dpp v30, v30, v30 quad_perm:[2,3,0,1] row_mask:0xf bank_mask:0xf
	s_nop 1
	v_mov_b32_e32 v31, v30
	s_nop 1
	v_add_f32_dpp v30, v31, v30 row_shl:4 row_mask:0xf bank_mask:0x5
	s_nop 1
	v_add_f32_dpp v30, v31, v30 row_shr:4 row_mask:0xf bank_mask:0xa
	s_nop 1
	v_mov_b32_e32 v31, 0
	s_waitcnt lgkmcnt(0)
	v_add_f32_e32 v30, v30, v31
	v_mov_b32_e32 v31, 0
	s_waitcnt lgkmcnt(0)
	v_add_f32_e32 v30, v30, v31
	v_mov_b32_e32 v31, 0
	s_and_saveexec_b64 s[20:21], vcc
	s_cbranch_execz .LBB0_474
	s_waitcnt lgkmcnt(0)
	v_add_f32_e32 v30, v30, v31
	ds_write_b32 v103, v30 offset:2048
.LBB0_474:
	s_or_b64 exec, exec, s[20:21]
	s_waitcnt vmcnt(6)
	v_and_b32_e32 v59, 0xffff0000, v26
	v_and_b32_e32 v61, 0xffff0000, v27
	v_lshlrev_b32_e32 v60, 16, v26
	v_mul_f32_e32 v26, v59, v59
	v_lshlrev_b32_e32 v62, 16, v27
	v_mul_f32_e32 v27, v61, v61
	v_fmac_f32_e32 v26, v60, v60
	v_fmac_f32_e32 v27, v62, v62
	v_and_b32_e32 v63, 0xffff0000, v28
	v_add_f32_e32 v26, v26, v27
	v_lshlrev_b32_e32 v64, 16, v28
	v_mul_f32_e32 v27, v63, v63
	v_fmac_f32_e32 v27, v64, v64
	v_and_b32_e32 v65, 0xffff0000, v29
	v_add_f32_e32 v26, v27, v26
	v_lshlrev_b32_e32 v66, 16, v29
	v_mul_f32_e32 v27, v65, v65
	v_fmac_f32_e32 v27, v66, v66
	v_add_f32_e32 v26, v27, v26
	s_nop 1
	v_add_f32_dpp v26, v26, v26 quad_perm:[1,0,3,2] row_mask:0xf bank_mask:0xf
	s_nop 1
	v_add_f32_dpp v26, v26, v26 quad_perm:[2,3,0,1] row_mask:0xf bank_mask:0xf
	s_nop 1
	v_mov_b32_e32 v27, v26
	s_nop 1
	v_add_f32_dpp v26, v27, v26 row_shl:4 row_mask:0xf bank_mask:0x5
	s_nop 1
	v_add_f32_dpp v26, v27, v26 row_shr:4 row_mask:0xf bank_mask:0xa
	s_nop 1
	v_mov_b32_e32 v27, 0
	s_waitcnt lgkmcnt(0)
	v_add_f32_e32 v26, v26, v27
	v_mov_b32_e32 v27, 0
	s_waitcnt lgkmcnt(0)
	v_add_f32_e32 v26, v26, v27
	v_mov_b32_e32 v27, 0
	s_and_saveexec_b64 s[20:21], vcc
	s_cbranch_execz .LBB0_476
	s_waitcnt lgkmcnt(0)
	v_add_f32_e32 v26, v26, v27
	ds_write_b32 v103, v26 offset:2304
.LBB0_476:
	s_or_b64 exec, exec, s[20:21]
	s_waitcnt vmcnt(5)
	v_and_b32_e32 v51, 0xffff0000, v22
	v_and_b32_e32 v53, 0xffff0000, v23
	v_lshlrev_b32_e32 v52, 16, v22
	v_mul_f32_e32 v22, v51, v51
	v_lshlrev_b32_e32 v54, 16, v23
	v_mul_f32_e32 v23, v53, v53
	v_fmac_f32_e32 v22, v52, v52
	v_fmac_f32_e32 v23, v54, v54
	v_and_b32_e32 v55, 0xffff0000, v24
	v_add_f32_e32 v22, v22, v23
	v_lshlrev_b32_e32 v56, 16, v24
	v_mul_f32_e32 v23, v55, v55
	v_fmac_f32_e32 v23, v56, v56
	v_and_b32_e32 v57, 0xffff0000, v25
	v_add_f32_e32 v22, v23, v22
	v_lshlrev_b32_e32 v58, 16, v25
	v_mul_f32_e32 v23, v57, v57
	v_fmac_f32_e32 v23, v58, v58
	v_add_f32_e32 v22, v23, v22
	s_nop 1
	v_add_f32_dpp v22, v22, v22 quad_perm:[1,0,3,2] row_mask:0xf bank_mask:0xf
	s_nop 1
	v_add_f32_dpp v22, v22, v22 quad_perm:[2,3,0,1] row_mask:0xf bank_mask:0xf
	s_nop 1
	v_mov_b32_e32 v23, v22
	s_nop 1
	v_add_f32_dpp v22, v23, v22 row_shl:4 row_mask:0xf bank_mask:0x5
	s_nop 1
	v_add_f32_dpp v22, v23, v22 row_shr:4 row_mask:0xf bank_mask:0xa
	s_nop 1
	v_mov_b32_e32 v23, 0
	s_waitcnt lgkmcnt(0)
	v_add_f32_e32 v22, v22, v23
	v_mov_b32_e32 v23, 0
	s_waitcnt lgkmcnt(0)
	v_add_f32_e32 v22, v22, v23
	v_mov_b32_e32 v23, 0
	s_and_saveexec_b64 s[20:21], vcc
	s_cbranch_execz .LBB0_478
	s_waitcnt lgkmcnt(0)
	v_add_f32_e32 v22, v22, v23
	ds_write_b32 v103, v22 offset:2560
.LBB0_478:
	s_or_b64 exec, exec, s[20:21]
	s_waitcnt vmcnt(4)
	v_and_b32_e32 v42, 0xffff0000, v18
	v_and_b32_e32 v44, 0xffff0000, v19
	v_lshlrev_b32_e32 v43, 16, v18
	v_mul_f32_e32 v18, v42, v42
	v_lshlrev_b32_e32 v45, 16, v19
	v_mul_f32_e32 v19, v44, v44
	v_fmac_f32_e32 v18, v43, v43
	v_fmac_f32_e32 v19, v45, v45
	v_and_b32_e32 v46, 0xffff0000, v20
	v_add_f32_e32 v18, v18, v19
	v_lshlrev_b32_e32 v47, 16, v20
	v_mul_f32_e32 v19, v46, v46
	v_fmac_f32_e32 v19, v47, v47
	v_and_b32_e32 v48, 0xffff0000, v21
	v_add_f32_e32 v18, v19, v18
	v_lshlrev_b32_e32 v50, 16, v21
	v_mul_f32_e32 v19, v48, v48
	v_fmac_f32_e32 v19, v50, v50
	v_add_f32_e32 v18, v19, v18
	s_nop 1
	v_add_f32_dpp v18, v18, v18 quad_perm:[1,0,3,2] row_mask:0xf bank_mask:0xf
	s_nop 1
	v_add_f32_dpp v18, v18, v18 quad_perm:[2,3,0,1] row_mask:0xf bank_mask:0xf
	s_nop 1
	v_mov_b32_e32 v19, v18
	s_nop 1
	v_add_f32_dpp v18, v19, v18 row_shl:4 row_mask:0xf bank_mask:0x5
	s_nop 1
	v_add_f32_dpp v18, v19, v18 row_shr:4 row_mask:0xf bank_mask:0xa
	s_nop 1
	v_mov_b32_e32 v19, 0
	s_waitcnt lgkmcnt(0)
	v_add_f32_e32 v18, v18, v19
	v_mov_b32_e32 v19, 0
	s_waitcnt lgkmcnt(0)
	v_add_f32_e32 v18, v18, v19
	v_mov_b32_e32 v19, 0
	s_and_saveexec_b64 s[20:21], vcc
	s_cbranch_execz .LBB0_480
	s_waitcnt lgkmcnt(0)
	v_add_f32_e32 v18, v18, v19
	ds_write_b32 v103, v18 offset:2816
.LBB0_480:
	s_or_b64 exec, exec, s[20:21]
	s_waitcnt vmcnt(3)
	v_and_b32_e32 v34, 0xffff0000, v14
	v_and_b32_e32 v36, 0xffff0000, v15
	v_lshlrev_b32_e32 v35, 16, v14
	v_mul_f32_e32 v14, v34, v34
	v_lshlrev_b32_e32 v37, 16, v15
	v_mul_f32_e32 v15, v36, v36
	v_fmac_f32_e32 v14, v35, v35
	v_fmac_f32_e32 v15, v37, v37
	v_and_b32_e32 v38, 0xffff0000, v16
	v_add_f32_e32 v14, v14, v15
	v_lshlrev_b32_e32 v39, 16, v16
	v_mul_f32_e32 v15, v38, v38
	v_fmac_f32_e32 v15, v39, v39
	v_and_b32_e32 v40, 0xffff0000, v17
	v_add_f32_e32 v14, v15, v14
	v_lshlrev_b32_e32 v41, 16, v17
	v_mul_f32_e32 v15, v40, v40
	v_fmac_f32_e32 v15, v41, v41
	v_add_f32_e32 v14, v15, v14
	s_nop 1
	v_add_f32_dpp v14, v14, v14 quad_perm:[1,0,3,2] row_mask:0xf bank_mask:0xf
	s_nop 1
	v_add_f32_dpp v14, v14, v14 quad_perm:[2,3,0,1] row_mask:0xf bank_mask:0xf
	s_nop 1
	v_mov_b32_e32 v15, v14
	s_nop 1
	v_add_f32_dpp v14, v15, v14 row_shl:4 row_mask:0xf bank_mask:0x5
	s_nop 1
	v_add_f32_dpp v14, v15, v14 row_shr:4 row_mask:0xf bank_mask:0xa
	s_nop 1
	v_mov_b32_e32 v15, 0
	s_waitcnt lgkmcnt(0)
	v_add_f32_e32 v14, v14, v15
	v_mov_b32_e32 v15, 0
	s_waitcnt lgkmcnt(0)
	v_add_f32_e32 v14, v14, v15
	v_mov_b32_e32 v15, 0
	s_and_saveexec_b64 s[20:21], vcc
	s_cbranch_execz .LBB0_482
	s_waitcnt lgkmcnt(0)
	v_add_f32_e32 v14, v14, v15
	ds_write_b32 v103, v14 offset:3072
.LBB0_482:
	s_or_b64 exec, exec, s[20:21]
	s_waitcnt vmcnt(2)
	v_and_b32_e32 v26, 0xffff0000, v10
	v_and_b32_e32 v28, 0xffff0000, v11
	v_lshlrev_b32_e32 v27, 16, v10
	v_mul_f32_e32 v10, v26, v26
	v_lshlrev_b32_e32 v29, 16, v11
	v_mul_f32_e32 v11, v28, v28
	v_fmac_f32_e32 v10, v27, v27
	v_fmac_f32_e32 v11, v29, v29
	v_and_b32_e32 v30, 0xffff0000, v12
	v_add_f32_e32 v10, v10, v11
	v_lshlrev_b32_e32 v31, 16, v12
	v_mul_f32_e32 v11, v30, v30
	v_fmac_f32_e32 v11, v31, v31
	v_and_b32_e32 v32, 0xffff0000, v13
	v_add_f32_e32 v10, v11, v10
	v_lshlrev_b32_e32 v33, 16, v13
	v_mul_f32_e32 v11, v32, v32
	v_fmac_f32_e32 v11, v33, v33
	v_add_f32_e32 v10, v11, v10
	s_nop 1
	v_add_f32_dpp v10, v10, v10 quad_perm:[1,0,3,2] row_mask:0xf bank_mask:0xf
	s_nop 1
	v_add_f32_dpp v10, v10, v10 quad_perm:[2,3,0,1] row_mask:0xf bank_mask:0xf
	s_nop 1
	v_mov_b32_e32 v11, v10
	s_nop 1
	v_add_f32_dpp v10, v11, v10 row_shl:4 row_mask:0xf bank_mask:0x5
	s_nop 1
	v_add_f32_dpp v10, v11, v10 row_shr:4 row_mask:0xf bank_mask:0xa
	s_nop 1
	v_mov_b32_e32 v11, 0
	s_waitcnt lgkmcnt(0)
	v_add_f32_e32 v10, v10, v11
	v_mov_b32_e32 v11, 0
	s_waitcnt lgkmcnt(0)
	v_add_f32_e32 v10, v10, v11
	v_mov_b32_e32 v11, 0
	s_and_saveexec_b64 s[20:21], vcc
	s_cbranch_execz .LBB0_484
	s_waitcnt lgkmcnt(0)
	v_add_f32_e32 v10, v10, v11
	ds_write_b32 v103, v10 offset:3328
.LBB0_484:
	s_or_b64 exec, exec, s[20:21]
	s_waitcnt vmcnt(1)
	v_and_b32_e32 v18, 0xffff0000, v6
	v_and_b32_e32 v20, 0xffff0000, v7
	v_lshlrev_b32_e32 v19, 16, v6
	v_mul_f32_e32 v6, v18, v18
	v_lshlrev_b32_e32 v21, 16, v7
	v_mul_f32_e32 v7, v20, v20
	v_fmac_f32_e32 v6, v19, v19
	v_fmac_f32_e32 v7, v21, v21
	v_and_b32_e32 v22, 0xffff0000, v8
	v_add_f32_e32 v6, v6, v7
	v_lshlrev_b32_e32 v23, 16, v8
	v_mul_f32_e32 v7, v22, v22
	v_fmac_f32_e32 v7, v23, v23
	v_and_b32_e32 v24, 0xffff0000, v9
	v_add_f32_e32 v6, v7, v6
	v_lshlrev_b32_e32 v25, 16, v9
	v_mul_f32_e32 v7, v24, v24
	v_fmac_f32_e32 v7, v25, v25
	v_add_f32_e32 v6, v7, v6
	s_nop 1
	v_add_f32_dpp v6, v6, v6 quad_perm:[1,0,3,2] row_mask:0xf bank_mask:0xf
	s_nop 1
	v_add_f32_dpp v6, v6, v6 quad_perm:[2,3,0,1] row_mask:0xf bank_mask:0xf
	s_nop 1
	v_mov_b32_e32 v7, v6
	s_nop 1
	v_add_f32_dpp v6, v7, v6 row_shl:4 row_mask:0xf bank_mask:0x5
	s_nop 1
	v_add_f32_dpp v6, v7, v6 row_shr:4 row_mask:0xf bank_mask:0xa
	s_nop 1
	v_mov_b32_e32 v7, 0
	s_waitcnt lgkmcnt(0)
	v_add_f32_e32 v6, v6, v7
	v_mov_b32_e32 v7, 0
	s_waitcnt lgkmcnt(0)
	v_add_f32_e32 v6, v6, v7
	v_mov_b32_e32 v7, 0
	s_and_saveexec_b64 s[20:21], vcc
	s_cbranch_execz .LBB0_486
	s_waitcnt lgkmcnt(0)
	v_add_f32_e32 v6, v6, v7
	ds_write_b32 v103, v6 offset:3584
.LBB0_486:
	s_or_b64 exec, exec, s[20:21]
	s_waitcnt vmcnt(0)
	v_and_b32_e32 v10, 0xffff0000, v2
	v_and_b32_e32 v12, 0xffff0000, v3
	v_lshlrev_b32_e32 v11, 16, v2
	v_mul_f32_e32 v2, v10, v10
	v_lshlrev_b32_e32 v13, 16, v3
	v_mul_f32_e32 v3, v12, v12
	v_fmac_f32_e32 v2, v11, v11
	v_fmac_f32_e32 v3, v13, v13
	v_and_b32_e32 v14, 0xffff0000, v4
	v_add_f32_e32 v2, v2, v3
	v_lshlrev_b32_e32 v15, 16, v4
	v_mul_f32_e32 v3, v14, v14
	v_fmac_f32_e32 v3, v15, v15
	v_and_b32_e32 v16, 0xffff0000, v5
	v_add_f32_e32 v2, v3, v2
	v_lshlrev_b32_e32 v17, 16, v5
	v_mul_f32_e32 v3, v16, v16
	v_fmac_f32_e32 v3, v17, v17
	v_add_f32_e32 v2, v3, v2
	s_nop 1
	v_add_f32_dpp v2, v2, v2 quad_perm:[1,0,3,2] row_mask:0xf bank_mask:0xf
	s_nop 1
	v_add_f32_dpp v2, v2, v2 quad_perm:[2,3,0,1] row_mask:0xf bank_mask:0xf
	s_nop 1
	v_mov_b32_e32 v3, v2
	s_nop 1
	v_add_f32_dpp v2, v3, v2 row_shl:4 row_mask:0xf bank_mask:0x5
	s_nop 1
	v_add_f32_dpp v2, v3, v2 row_shr:4 row_mask:0xf bank_mask:0xa
	s_nop 1
	v_mov_b32_e32 v3, 0
	s_waitcnt lgkmcnt(0)
	v_add_f32_e32 v2, v2, v3
	v_mov_b32_e32 v3, 0
	s_waitcnt lgkmcnt(0)
	v_add_f32_e32 v2, v2, v3
	v_mov_b32_e32 v3, 0
	s_and_saveexec_b64 s[20:21], vcc
	s_cbranch_execz .LBB0_488
	s_waitcnt lgkmcnt(0)
	v_add_f32_e32 v2, v2, v3
	ds_write_b32 v103, v2 offset:3840
